# K LDS images with swizzles that are conflict-free for ds_read_b128 lane groups ((row&15)<<4 nope, ((row>>1)&7)<<4 rope)
# speedup vs baseline: 1.0212x; 1.0120x over previous
.LBB0_744:
	s_or_b64 exec, exec, s[4:5]
	v_mbcnt_lo_u32_b32 v0, -1, 0
	v_mbcnt_hi_u32_b32 v0, -1, v0
	s_mov_b32 s36, s2
	v_add_u32_e32 v254, s3, v0
	s_mov_b64 s[4:5], s[0:1]
	s_cmpk_gt_i32 s36, 0x21f
	s_cbranch_scc1 .LBB0_773
	s_load_dwordx2 s[4:5], s[4:5], 0x100
	v_ashrrev_i32_e32 v142, 4, v254
	v_add_u32_e32 v11, 32, v142
	v_and_b32_e32 v6, 0xfffff0, v142
	v_lshlrev_b32_e32 v7, 1, v142
	s_waitcnt lgkmcnt(0)
	s_add_u32 s37, s4, 0x2d380000
	s_addc_u32 s38, s5, 0
	s_add_u32 s39, s4, 0x30680000
	s_addc_u32 s40, s5, 0
	s_add_u32 s41, s4, 0x33980000
	s_addc_u32 s42, s5, 0
	v_and_b32_e32 v12, 0xfffff0, v11
	v_lshlrev_b32_e32 v13, 1, v11
	s_add_u32 s43, s4, 0x35b80000
	v_lshlrev_b32_e32 v4, 3, v254
	v_and_or_b32 v6, v7, 8, v6
	v_and_or_b32 v12, v13, 8, v12
	s_addc_u32 s44, s5, 0
	v_and_b32_e32 v2, 0x78, v4
	v_lshrrev_b32_e32 v7, 1, v142
	v_lshrrev_b32_e32 v6, 1, v6
	v_bfe_u32 v8, v4, 5, 2
	v_and_b32_e32 v9, 3, v142
	v_lshrrev_b32_e32 v12, 1, v12
	v_and_b32_e32 v1, 63, v254
	s_cmpk_lg_i32 s29, 0x100
	v_or_b32_e32 v6, v6, v8
	v_and_or_b32 v7, v7, 4, v9
	v_lshlrev_b32_e32 v9, 1, v2
	v_or_b32_e32 v8, v12, v8
	s_cselect_b64 s[24:25], -1, 0
	v_lshlrev_b32_e32 v5, 4, v1
	s_add_i32 s4, 0, 0x14800
	v_lshlrev_b32_e32 v6, 9, v6
	v_lshlrev_b32_e32 v7, 6, v7
	v_and_b32_e32 v10, 48, v9
	v_lshlrev_b32_e32 v8, 9, v8
	v_add_u32_e32 v166, s4, v5
	v_or3_b32 v6, v6, v7, v10
	v_or3_b32 v7, v8, v7, v10
	v_lshlrev_b32_e32 v8, 3, v1
	v_and_b32_e32 v5, 0xc0, v5
	v_lshlrev_b32_e32 v10, 1, v254
	v_ashrrev_i32_e32 v144, 3, v254
	v_and_or_b32 v5, v8, 24, v5
	v_and_b32_e32 v10, 32, v10
	v_and_b32_e32 v8, 0x100, v8
	v_and_b32_e32 v4, 56, v4
	v_or3_b32 v5, v5, v10, v8
	v_lshlrev_b32_e32 v8, 8, v142
	v_and_b32_e32 v10, 0x70, v254
	v_lshlrev_b32_e32 v11, 8, v11
	v_lshlrev_b32_e32 v12, 4, v144
	v_bfe_u32 v3, v254, 5, 1
	v_bitop3_b32 v8, v9, v8, v10 bitop3:0xde
	v_bitop3_b32 v9, v9, v11, v10 bitop3:0xde
	v_lshlrev_b32_e32 v10, 7, v144
	v_lshlrev_b32_e32 v11, 1, v4
	v_and_b32_e32 v12, 0x70, v12
	v_and_b32_e32 v188, 31, v254
	s_cmp_lg_u32 0, -1
	v_bitop3_b32 v168, v11, v10, v12 bitop3:0xde
	v_lshlrev_b32_e32 v169, 4, v3
	v_lshlrev_b32_e32 v10, 4, v254
	v_lshlrev_b32_e32 v0, 3, v3
	s_cselect_b32 s6, 0, 0
	v_lshlrev_b32_e32 v3, 8, v188
	v_and_b32_e32 v10, 0x70, v10
	v_or_b32_e32 v12, 32, v169
	v_or_b32_e32 v14, 64, v169
	v_or_b32_e32 v16, 0x60, v169
	v_or_b32_e32 v18, 0x80, v169
	v_or_b32_e32 v19, 0xa0, v169
	v_or_b32_e32 v20, 0xc0, v169
	v_or_b32_e32 v21, 0xe0, v169
	v_mov_b32_e32 v141, 0
	v_add_u32_e32 v167, s6, v5
	v_ashrrev_i32_e32 v143, 31, v142
	v_bitop3_b32 v11, v169, v3, v10 bitop3:0xde
	v_bitop3_b32 v13, v12, v3, v10 bitop3:0xde
	v_bitop3_b32 v15, v14, v3, v10 bitop3:0xde
	v_bitop3_b32 v17, v16, v3, v10 bitop3:0xde
	v_bitop3_b32 v18, v18, v3, v10 bitop3:0xde
	v_bitop3_b32 v19, v19, v3, v10 bitop3:0xde
	v_bitop3_b32 v20, v20, v3, v10 bitop3:0xde
	v_bitop3_b32 v3, v21, v3, v10 bitop3:0xde
	v_lshlrev_b32_e32 v21, 7, v188
	s_addk_i32 s6, 0x4000
	s_add_i32 s47, 0, 0x10000
	s_mov_b32 s27, 0
	v_lshl_add_u64 v[146:147], v[142:143], 0, 32
	v_ashrrev_i32_e32 v145, 31, v144
	v_bitop3_b32 v170, v169, v21, v10 bitop3:0xde
	v_bitop3_b32 v171, v12, v21, v10 bitop3:0xde
	v_bitop3_b32 v172, v14, v21, v10 bitop3:0xde
	v_bitop3_b32 v173, v16, v21, v10 bitop3:0xde
	v_cmp_gt_u32_e64 s[4:5], 32, v1
	s_movk_i32 s45, 0x4000
	v_add_u32_e32 v174, s6, v5
	s_movk_i32 s46, 0xc00
	v_lshlrev_b32_e32 v148, 1, v0
	v_lshlrev_b32_e32 v150, 1, v2
	v_lshlrev_b32_e32 v152, 1, v4
	v_mov_b32_e32 v153, v141
	s_mov_b32 s48, 0x42ddb3d8
	s_mov_b32 s28, 0x3dd53b94
	s_movk_i32 s49, 0x1000
	s_movk_i32 s50, 0x5000
	s_mov_b32 s51, 0x8000
	s_mov_b32 s58, 0x9000
	s_mov_b32 s59, 0xc000
	s_mov_b32 s60, 0xd000
	v_mov_b32_e32 v149, v141
	v_mov_b32_e32 v151, v141
	v_add_u32_e32 v175, 0, v6
	v_add_u32_e32 v176, 0, v7
	v_add_u32_e32 v177, 0, v8
	v_add_u32_e32 v178, 0, v9
	v_add_u32_e32 v179, s47, v168
	v_add_u32_e32 v180, 0, v11
	v_add_u32_e32 v181, 0, v13
	v_add_u32_e32 v182, 0, v15
	v_add_u32_e32 v183, 0, v17
	v_add_u32_e32 v184, 0, v18
	v_add_u32_e32 v185, 0, v19
	v_add_u32_e32 v186, 0, v20
	v_add_u32_e32 v187, 0, v3
	v_and_b32_e32 v190, 15, v188
	v_lshlrev_b32_e32 v190, 4, v190
	v_xor_b32_e32 v190, v190, v169
	v_lshlrev_b32_e32 v192, 8, v188
	v_mov_b32_e32 v191, v190
	v_or_b32_e32 v180, v192, v191
	v_xor_b32_e32 v191, 0x20, v190
	v_or_b32_e32 v181, v192, v191
	v_xor_b32_e32 v191, 0x40, v190
	v_or_b32_e32 v182, v192, v191
	v_xor_b32_e32 v191, 0x60, v190
	v_or_b32_e32 v183, v192, v191
	v_xor_b32_e32 v191, 0x80, v190
	v_or_b32_e32 v184, v192, v191
	v_xor_b32_e32 v191, 0xa0, v190
	v_or_b32_e32 v185, v192, v191
	v_xor_b32_e32 v191, 0xc0, v190
	v_or_b32_e32 v186, v192, v191
	v_xor_b32_e32 v191, 0xe0, v190
	v_or_b32_e32 v187, v192, v191
	v_bfe_u32 v190, v188, 1, 3
	v_lshlrev_b32_e32 v190, 4, v190
	v_xor_b32_e32 v190, v190, v169
	v_lshlrev_b32_e32 v192, 7, v188
	v_mov_b32_e32 v191, v190
	v_add_u32_e32 v170, v192, v191
	v_xor_b32_e32 v191, 0x20, v190
	v_add_u32_e32 v171, v192, v191
	v_xor_b32_e32 v191, 0x40, v190
	v_add_u32_e32 v172, v192, v191
	v_xor_b32_e32 v191, 0x60, v190
	v_add_u32_e32 v173, v192, v191
	v_and_b32_e32 v190, 15, v142
	v_and_b32_e32 v191, 15, v254
	v_xor_b32_e32 v190, v190, v191
	v_lshlrev_b32_e32 v190, 4, v190
	v_lshl_add_u32 v177, v142, 8, v190
	v_add_u32_e32 v178, 0x2000, v177
	v_bfe_u32 v190, v144, 1, 3
	v_and_b32_e32 v191, 7, v254
	v_xor_b32_e32 v190, v190, v191
	v_lshlrev_b32_e32 v190, 4, v190
	v_lshl_add_u32 v168, v144, 7, v190
	v_add_u32_e32 v179, s47, v168
	s_branch .LBB0_747

.LBB0_756:
	s_and_b32 s8, s8, 7
	s_ashr_i32 s31, s30, 31
	s_mul_i32 s7, s30, 0xc00
	s_mul_hi_i32 s6, s30, 0xc00
	s_add_u32 s7, s37, s7
	s_addc_u32 s6, s38, s6
	s_mul_i32 s9, s8, 0x180
	s_add_u32 s10, s7, s9
	s_addc_u32 s11, s6, 0
	s_add_u32 s6, s39, s9
	s_addc_u32 s7, s40, 0
	s_lshl_b32 s61, s8, 7
	s_lshl_b32 s8, s8, 8
	s_add_u32 s34, s41, s8
	v_readfirstlane_b32 s9, v254
	s_addc_u32 s35, s42, 0
	s_ashr_i32 s8, s9, 6
	s_lshl_b32 s82, s8, 10
	s_mov_b32 s72, s6
	s_and_b32 s73, s7, 0xffff
	s_mov_b32 s74, 0x7ffffff0
	s_mov_b32 s75, 0x20000
	s_mov_b32 s76, s34
	s_and_b32 s77, s35, 0xffff
	s_mov_b32 s78, 0x7ffffff0
	s_mov_b32 s79, 0x20000
	v_lshl_or_b32 v2, s8, 5, v188
	v_mov_b64_e32 v[0:1], s[10:11]
	v_mad_i64_i32 v[0:1], s[10:11], v2, s46, v[0:1]
	v_lshl_add_u64 v[26:27], s[26:27], 0, v[142:143]
	v_lshl_add_u64 v[28:29], v[146:147], 0, s[26:27]
	v_lshl_add_u64 v[38:39], v[0:1], 0, v[148:149]
	v_lshlrev_b64 v[0:1], 11, v[26:27]
	v_lshlrev_b64 v[18:19], 11, v[28:29]
	v_lshl_add_u64 v[0:1], s[34:35], 0, v[0:1]
	v_lshl_add_u64 v[18:19], s[34:35], 0, v[18:19]
	v_lshl_add_u64 v[0:1], v[0:1], 0, v[150:151]
	v_lshl_add_u64 v[22:23], v[18:19], 0, v[150:151]
	global_load_dwordx4 v[2:5], v[38:39], off offset:256
	global_load_dwordx4 v[6:9], v[38:39], off offset:288
	global_load_dwordx4 v[10:13], v[38:39], off offset:320
	global_load_dwordx4 v[14:17], v[38:39], off offset:352
	global_load_dwordx4 v[18:21], v[0:1], off
	s_nop 0
	global_load_dwordx4 v[22:25], v[22:23], off
	v_mov_b64_e32 v[0:1], s[6:7]
	v_mad_u64_u32 v[30:31], s[10:11], v26, s46, v[0:1]
	v_mad_i32_i24 v31, v27, s46, v31
	v_lshl_add_u64 v[26:27], v[30:31], 0, v[150:151]
	v_mad_u64_u32 v[30:31], s[10:11], v28, s46, v[0:1]
	v_mad_i32_i24 v31, v29, s46, v31
	v_lshl_add_u64 v[30:31], v[30:31], 0, v[150:151]
	v_lshl_add_u64 v[34:35], s[26:27], 0, v[144:145]
	global_load_dwordx4 v[26:29], v[26:27], off
	s_nop 0
	global_load_dwordx4 v[30:33], v[30:31], off
	v_mad_u64_u32 v[36:37], s[10:11], v34, s46, v[0:1]
	v_mad_i32_i24 v37, v35, s46, v37
	v_lshl_add_u64 v[34:35], v[36:37], 0, v[152:153]
	global_load_dwordx4 v[34:37], v[34:35], off offset:256
	s_nop 0
	global_load_dwordx4 v[124:127], v[38:39], off
	global_load_dwordx4 v[120:123], v[38:39], off offset:32
	global_load_dwordx4 v[116:119], v[38:39], off offset:64
	global_load_dwordx4 v[112:115], v[38:39], off offset:96
	global_load_dwordx4 v[108:111], v[38:39], off offset:128
	global_load_dwordx4 v[104:107], v[38:39], off offset:160
	global_load_dwordx4 v[100:103], v[38:39], off offset:192
	global_load_dwordx4 v[96:99], v[38:39], off offset:224
	s_lshl_b32 s8, s8, 12
	v_add_u32_e32 v190, s8, v166
	v_add_u32_e32 v191, s47, v170
	v_add_u32_e32 v192, s47, v171
	v_add_u32_e32 v193, s47, v172
	v_add_u32_e32 v194, s47, v173
	s_and_b32 s9, s9, 0x3fffffc0
	s_lshl_b32 s9, s9, 2
	s_add_i32 s62, s9, 0
	s_add_i32 s62, s62, 0x14000
	s_mov_b32 s11, s27
	s_mov_b32 s22, s27
	s_mov_b32 s23, s27
	s_mov_b32 s8, s27
	s_mov_b32 s9, s27
	s_mov_b32 s12, s27
	s_mov_b32 s13, s27
	s_mov_b32 s14, s27
	s_mov_b32 s15, s27
	s_mov_b32 s16, s27
	s_mov_b32 s17, s27
	s_mov_b32 s18, s27
	s_mov_b32 s19, s27
	s_mov_b32 s20, s27
	s_mov_b32 s21, s27
	v_add_u32_e32 v195, 0, v168
	s_mov_b32 s64, 2
	v_mov_b32_e32 v140, 0
	v_add_u32_e32 v196, 0x12000, v195
	v_lshrrev_b32_e32 v156, 4, v254
	v_and_b32_e32 v157, 15, v156
	v_and_b32_e32 v159, 15, v254
	v_xor_b32_e32 v157, v157, v159
	v_lshlrev_b32_e32 v157, 4, v157
	v_mad_u32_u24 v154, v156, s46, v157
	v_lshrrev_b32_e32 v156, 3, v254
	v_bfe_u32 v157, v254, 4, 3
	v_and_b32_e32 v159, 7, v254
	v_xor_b32_e32 v157, v157, v159
	v_lshlrev_b32_e32 v157, 4, v157
	v_add_u32_e32 v157, 0x100, v157
	v_mad_u32_u24 v155, v156, s46, v157
	v_and_b32_e32 v158, 3, v254
	v_lshlrev_b32_e32 v158, 4, v158
	v_bfe_u32 v156, v254, 5, 2
	v_lshl_or_b32 v158, v156, 6, v158
	v_bfe_u32 v156, v254, 2, 2
	v_lshl_or_b32 v158, v156, 11, v158
	v_bfe_u32 v156, v254, 7, 1
	v_lshl_or_b32 v158, v156, 13, v158
	v_bfe_u32 v156, v254, 4, 1
	v_lshl_or_b32 v158, v156, 14, v158
	v_bfe_u32 v156, v254, 8, 1
	v_lshl_or_b32 v158, v156, 15, v158
	v_lshl_add_u32 v189, v188, 2, s62
	s_waitcnt vmcnt(16)
	ds_write_b128 v190, v[2:5]
	s_waitcnt vmcnt(15)
	ds_write_b128 v190, v[6:9] offset:1024
	s_waitcnt vmcnt(14)
	ds_write_b128 v190, v[10:13] offset:2048
	s_waitcnt vmcnt(13)
	ds_write_b128 v190, v[14:17] offset:3072
	s_waitcnt vmcnt(0)
	s_waitcnt vmcnt(12)
	ds_write_b128 v175, v[18:21]
	s_waitcnt vmcnt(11)
	ds_write_b128 v176, v[22:25]
	s_waitcnt vmcnt(10)
	ds_write_b128 v177, v[26:29] offset:32768
	s_waitcnt vmcnt(9)
	ds_write_b128 v178, v[30:33] offset:32768
	s_waitcnt vmcnt(8)
	ds_write_b128 v179, v[34:37]
	s_waitcnt lgkmcnt(0)
	s_barrier
	ds_read_b128 v[2:5], v180 offset:32768
	ds_read_b128 v[6:9], v180 offset:40960
	s_waitcnt vmcnt(7) lgkmcnt(1)
	v_mfma_f32_32x32x16_bf16 v[48:63], v[2:5], v[124:127], 0
	s_waitcnt lgkmcnt(0)
	v_mfma_f32_32x32x16_bf16 v[64:79], v[6:9], v[124:127], 0
	ds_read_b128 v[2:5], v181 offset:32768
	ds_read_b128 v[6:9], v181 offset:40960
	s_waitcnt vmcnt(6) lgkmcnt(1)
	v_mfma_f32_32x32x16_bf16 v[48:63], v[2:5], v[120:123], v[48:63]
	s_waitcnt lgkmcnt(0)
	v_mfma_f32_32x32x16_bf16 v[64:79], v[6:9], v[120:123], v[64:79]
	ds_read_b128 v[2:5], v182 offset:32768
	ds_read_b128 v[6:9], v182 offset:40960
	s_waitcnt vmcnt(5) lgkmcnt(1)
	v_mfma_f32_32x32x16_bf16 v[48:63], v[2:5], v[116:119], v[48:63]
	s_waitcnt lgkmcnt(0)
	v_mfma_f32_32x32x16_bf16 v[64:79], v[6:9], v[116:119], v[64:79]
	ds_read_b128 v[2:5], v183 offset:32768
	ds_read_b128 v[6:9], v183 offset:40960
	s_waitcnt vmcnt(4) lgkmcnt(1)
	v_mfma_f32_32x32x16_bf16 v[48:63], v[2:5], v[112:115], v[48:63]
	s_waitcnt lgkmcnt(0)
	v_mfma_f32_32x32x16_bf16 v[64:79], v[6:9], v[112:115], v[64:79]
	ds_read_b128 v[2:5], v184 offset:32768
	ds_read_b128 v[6:9], v184 offset:40960
	s_waitcnt vmcnt(3) lgkmcnt(1)
	v_mfma_f32_32x32x16_bf16 v[48:63], v[2:5], v[108:111], v[48:63]
	s_waitcnt lgkmcnt(0)
	v_mfma_f32_32x32x16_bf16 v[64:79], v[6:9], v[108:111], v[64:79]
	ds_read_b128 v[2:5], v185 offset:32768
	ds_read_b128 v[6:9], v185 offset:40960
	s_waitcnt vmcnt(2) lgkmcnt(1)
	v_mfma_f32_32x32x16_bf16 v[48:63], v[2:5], v[104:107], v[48:63]
	s_waitcnt lgkmcnt(0)
	v_mfma_f32_32x32x16_bf16 v[64:79], v[6:9], v[104:107], v[64:79]
	ds_read_b128 v[2:5], v186 offset:32768
	ds_read_b128 v[6:9], v186 offset:40960
	s_waitcnt vmcnt(1) lgkmcnt(1)
	v_mfma_f32_32x32x16_bf16 v[48:63], v[2:5], v[100:103], v[48:63]
	s_waitcnt lgkmcnt(0)
	v_mfma_f32_32x32x16_bf16 v[64:79], v[6:9], v[100:103], v[64:79]
	ds_read_b128 v[2:5], v187 offset:32768
	ds_read_b128 v[6:9], v187 offset:40960
	s_waitcnt vmcnt(0) lgkmcnt(1)
	v_mfma_f32_32x32x16_bf16 v[48:63], v[2:5], v[96:99], v[48:63]
	s_waitcnt lgkmcnt(0)
	v_mfma_f32_32x32x16_bf16 v[64:79], v[6:9], v[96:99], v[64:79]
	ds_read_b128 v[2:5], v191
	ds_read_b128 v[6:9], v190
	ds_read_b128 v[10:13], v191 offset:4096
	ds_read_b128 v[14:17], v190 offset:1024
	s_waitcnt lgkmcnt(2)
	v_mfma_f32_32x32x16_bf16 v[48:63], v[2:5], v[6:9], v[48:63]
	s_waitcnt lgkmcnt(1)
	v_mfma_f32_32x32x16_bf16 v[64:79], v[10:13], v[6:9], v[64:79]
	ds_read_b128 v[2:5], v192
	ds_read_b128 v[6:9], v192 offset:4096
	s_waitcnt lgkmcnt(1)
	v_mfma_f32_32x32x16_bf16 v[48:63], v[2:5], v[14:17], v[48:63]
	s_waitcnt lgkmcnt(0)
	v_mfma_f32_32x32x16_bf16 v[64:79], v[6:9], v[14:17], v[64:79]
	ds_read_b128 v[2:5], v193
	ds_read_b128 v[6:9], v190 offset:2048
	ds_read_b128 v[10:13], v193 offset:4096
	ds_read_b128 v[14:17], v190 offset:3072
	s_waitcnt lgkmcnt(2)
	v_mfma_f32_32x32x16_bf16 v[48:63], v[2:5], v[6:9], v[48:63]
	s_waitcnt lgkmcnt(1)
	v_mfma_f32_32x32x16_bf16 v[64:79], v[10:13], v[6:9], v[64:79]
	ds_read_b128 v[2:5], v194
	ds_read_b128 v[6:9], v194 offset:4096
	s_waitcnt lgkmcnt(1)
	v_mfma_f32_32x32x16_bf16 v[48:63], v[2:5], v[14:17], v[48:63]
	s_waitcnt lgkmcnt(0)
	v_mfma_f32_32x32x16_bf16 v[64:79], v[6:9], v[14:17], v[64:79]
	s_nop 9
	v_max_f32_e32 v2, v49, v49
	v_max_f32_e32 v3, v48, v48
	v_max_f32_e32 v2, v3, v2
	v_max3_f32 v2, v2, v50, v51
	v_max3_f32 v2, v2, v52, v53
	v_max3_f32 v2, v2, v54, v55
	v_max3_f32 v2, v2, v56, v57
	v_max3_f32 v2, v2, v58, v59
	v_max3_f32 v2, v2, v60, v61
	v_max3_f32 v2, v2, v62, v63
	v_max3_f32 v2, v2, v64, v65
	v_max3_f32 v2, v2, v66, v67
	v_max3_f32 v2, v2, v68, v69
	v_max3_f32 v2, v2, v70, v71
	v_max3_f32 v2, v2, v72, v73
	v_max3_f32 v2, v2, v74, v75
	v_max3_f32 v2, v2, v76, v77
	v_max3_f32 v2, v2, v78, v79
	v_mov_b32_e32 v3, v2
	s_nop 1
	v_permlane32_swap_b32_e32 v2, v3
	v_max_f32_e32 v3, v3, v3
	v_max_f32_e32 v2, v2, v2
	v_max_f32_e32 v2, v2, v3
	v_add_f32_e32 v3, 0x7149f2ca, v2
	v_cmp_ge_f32_e32 vcc, s48, v3
	s_cmp_eq_u64 vcc, exec
	s_cselect_b64 vcc, -1, 0
	s_add_i32 s10, s26, 64
	v_max_f32_e32 v128, 0xf149f2ca, v2
	v_lshl_add_u64 v[2:3], s[10:11], 0, v[142:143]
	v_lshl_add_u64 v[4:5], v[146:147], 0, s[10:11]
	v_lshl_add_u64 v[6:7], s[10:11], 0, v[144:145]
	v_lshlrev_b64 v[8:9], 11, v[2:3]
	v_lshlrev_b64 v[10:11], 11, v[4:5]
	v_mad_u64_u32 v[12:13], s[10:11], v2, s46, v[0:1]
	v_mad_u64_u32 v[14:15], s[10:11], v4, s46, v[0:1]
	v_mad_u64_u32 v[0:1], s[10:11], v6, s46, v[0:1]
	v_lshl_add_u64 v[8:9], s[34:35], 0, v[8:9]
	v_lshl_add_u64 v[10:11], s[34:35], 0, v[10:11]
	v_mad_i32_i24 v13, v3, s46, v13
	v_mad_i32_i24 v15, v5, s46, v15
	v_mad_i32_i24 v1, v7, s46, v1
	v_lshl_add_u64 v[2:3], v[8:9], 0, v[150:151]
	v_lshl_add_u64 v[4:5], v[10:11], 0, v[150:151]
	v_lshl_add_u64 v[6:7], v[12:13], 0, v[150:151]
	v_lshl_add_u64 v[8:9], v[14:15], 0, v[150:151]
	v_lshl_add_u64 v[0:1], v[0:1], 0, v[152:153]
	global_load_dwordx4 v[80:83], v[2:3], off
	global_load_dwordx4 v[84:87], v[4:5], off
	global_load_dwordx4 v[88:91], v[6:7], off
	global_load_dwordx4 v[92:95], v[8:9], off
	global_load_dwordx4 v[200:203], v[0:1], off offset:256
	v_sub_f32_e32 v129, 0xf149f2ca, v128
	v_mul_f32_e32 v129, 0x3dd53b94, v129
	v_exp_f32_e32 v164, v129
	v_mov_b32_e32 v129, 0xf149f2ca
	v_cndmask_b32_e32 v198, v128, v129, vcc
	v_mul_f32_e32 v138, 0xbdd53b94, v198
	v_mov_b32_e32 v165, v138
	v_fmamk_f32 v48, v48, 0x3dd53b94, v138
	v_fmamk_f32 v49, v49, 0x3dd53b94, v138
	v_fmamk_f32 v50, v50, 0x3dd53b94, v138
	v_fmamk_f32 v51, v51, 0x3dd53b94, v138
	v_fmamk_f32 v52, v52, 0x3dd53b94, v138
	v_fmamk_f32 v53, v53, 0x3dd53b94, v138
	v_fmamk_f32 v54, v54, 0x3dd53b94, v138
	v_fmamk_f32 v55, v55, 0x3dd53b94, v138
	v_fmamk_f32 v56, v56, 0x3dd53b94, v138
	v_fmamk_f32 v57, v57, 0x3dd53b94, v138
	v_fmamk_f32 v58, v58, 0x3dd53b94, v138
	v_fmamk_f32 v59, v59, 0x3dd53b94, v138
	v_fmamk_f32 v60, v60, 0x3dd53b94, v138
	v_fmamk_f32 v61, v61, 0x3dd53b94, v138
	v_fmamk_f32 v62, v62, 0x3dd53b94, v138
	v_fmac_f32_e32 v165, 0x3dd53b94, v63
	s_mov_b32 s10, s27
	s_mov_b32 s11, s27
	v_mov_b64_e32 v[30:31], s[22:23]
	v_exp_f32_e32 v222, v48
	v_exp_f32_e32 v224, v49
	v_exp_f32_e32 v220, v50
	v_exp_f32_e32 v223, v51
	v_exp_f32_e32 v219, v52
	v_exp_f32_e32 v221, v53
	v_exp_f32_e32 v217, v54
	v_exp_f32_e32 v218, v55
	v_exp_f32_e32 v212, v56
	v_exp_f32_e32 v214, v57
	v_exp_f32_e32 v211, v58
	v_exp_f32_e32 v213, v59
	v_exp_f32_e32 v208, v60
	v_exp_f32_e32 v210, v61
	v_exp_f32_e32 v207, v62
	v_exp_f32_e32 v209, v165
	v_mov_b64_e32 v[16:17], s[8:9]
	s_waitcnt vmcnt(0)
	v_mov_b64_e32 v[28:29], s[20:21]
	v_mov_b64_e32 v[26:27], s[18:19]
	v_mov_b64_e32 v[24:25], s[16:17]
	v_mov_b64_e32 v[22:23], s[14:15]
	v_mov_b64_e32 v[20:21], s[12:13]
	v_mov_b64_e32 v[18:19], s[10:11]
	v_mov_b64_e32 v[46:47], v[30:31]
	v_mov_b64_e32 v[0:1], v[16:17]
	v_mov_b64_e32 v[62:63], v[30:31]
	v_mov_b64_e32 v[44:45], v[28:29]
	v_mov_b64_e32 v[42:43], v[26:27]
	v_mov_b64_e32 v[40:41], v[24:25]
	v_mov_b64_e32 v[38:39], v[22:23]
	v_mov_b64_e32 v[36:37], v[20:21]
	v_mov_b64_e32 v[34:35], v[18:19]
	v_mov_b64_e32 v[32:33], v[16:17]
	v_mov_b64_e32 v[2:3], v[18:19]
	v_mov_b64_e32 v[4:5], v[20:21]
	v_mov_b64_e32 v[6:7], v[22:23]
	v_mov_b64_e32 v[8:9], v[24:25]
	v_mov_b64_e32 v[10:11], v[26:27]
	v_mov_b64_e32 v[12:13], v[28:29]
	v_mov_b64_e32 v[14:15], v[30:31]
	s_add_i32 s10, s26, 0x80
	s_add_i32 s83, s26, 64
	s_sub_i32 s11, s65, 64
	v_pk_fma_f32 v[134:135], v[78:79], s[28:29], v[138:139] op_sel_hi:[1,0,0]
	v_pk_fma_f32 v[160:161], v[76:77], s[28:29], v[138:139] op_sel_hi:[1,0,0]
	v_pk_fma_f32 v[162:163], v[74:75], s[28:29], v[138:139] op_sel_hi:[1,0,0]
	v_pk_fma_f32 v[128:129], v[72:73], s[28:29], v[138:139] op_sel_hi:[1,0,0]
	v_pk_fma_f32 v[130:131], v[70:71], s[28:29], v[138:139] op_sel_hi:[1,0,0]
	v_pk_fma_f32 v[132:133], v[68:69], s[28:29], v[138:139] op_sel_hi:[1,0,0]
	v_pk_fma_f32 v[136:137], v[66:67], s[28:29], v[138:139] op_sel_hi:[1,0,0]
	v_pk_fma_f32 v[138:139], v[64:65], s[28:29], v[138:139] op_sel_hi:[1,0,0]
	v_cndmask_b32_e64 v197, v164, 1.0, vcc
	v_mov_b64_e32 v[60:61], v[28:29]
	v_mov_b64_e32 v[58:59], v[26:27]
	v_mov_b64_e32 v[56:57], v[24:25]
	v_mov_b64_e32 v[54:55], v[22:23]
	v_mov_b64_e32 v[52:53], v[20:21]
	v_mov_b64_e32 v[50:51], v[18:19]
	v_mov_b64_e32 v[48:49], v[16:17]
	s_waitcnt vmcnt(4)
	ds_write_b128 v175, v[80:83] offset:16384
	s_waitcnt vmcnt(3)
	ds_write_b128 v176, v[84:87] offset:16384
	s_waitcnt vmcnt(2)
	ds_write_b128 v177, v[88:91] offset:49152
	s_waitcnt vmcnt(1)
	ds_write_b128 v178, v[92:95] offset:49152
	s_waitcnt vmcnt(0)
	ds_write_b128 v196, v[200:203]
	s_waitcnt lgkmcnt(0)
	s_barrier

.LBB0_2004:
	s_or_b64 exec, exec, s[4:5]
	v_mbcnt_lo_u32_b32 v0, -1, 0
	v_mbcnt_hi_u32_b32 v0, -1, v0
	s_mov_b32 s34, s2
	v_add_u32_e32 v254, s3, v0
	s_mov_b64 s[4:5], s[0:1]
	s_cmpk_gt_i32 s34, 0x1ff
	s_cbranch_scc1 .LBB0_2028
	s_load_dwordx2 s[4:5], s[4:5], 0x100
	v_ashrrev_i32_e32 v142, 4, v254
	v_add_u32_e32 v11, 32, v142
	v_and_b32_e32 v6, 0xfffff0, v142
	v_lshlrev_b32_e32 v7, 1, v142
	s_waitcnt lgkmcnt(0)
	s_add_u32 s35, s4, 0x2d380000
	s_addc_u32 s36, s5, 0
	s_add_u32 s37, s4, 0x30680000
	s_addc_u32 s38, s5, 0
	s_add_u32 s39, s4, 0x33980000
	s_addc_u32 s40, s5, 0
	v_and_b32_e32 v12, 0xfffff0, v11
	v_lshlrev_b32_e32 v13, 1, v11
	s_add_u32 s41, s4, 0x35b80000
	v_lshlrev_b32_e32 v4, 3, v254
	v_and_or_b32 v6, v7, 8, v6
	v_and_or_b32 v12, v13, 8, v12
	s_addc_u32 s42, s5, 0
	v_and_b32_e32 v2, 0x78, v4
	v_lshrrev_b32_e32 v7, 1, v142
	v_lshrrev_b32_e32 v6, 1, v6
	v_bfe_u32 v8, v4, 5, 2
	v_and_b32_e32 v9, 3, v142
	v_lshrrev_b32_e32 v12, 1, v12
	v_and_b32_e32 v1, 63, v254
	s_cmpk_lg_i32 s27, 0x100
	v_or_b32_e32 v6, v6, v8
	v_and_or_b32 v7, v7, 4, v9
	v_lshlrev_b32_e32 v9, 1, v2
	v_or_b32_e32 v8, v12, v8
	s_cselect_b64 s[24:25], -1, 0
	v_lshlrev_b32_e32 v5, 4, v1
	s_add_i32 s4, 0, 0x14800
	v_lshlrev_b32_e32 v6, 9, v6
	v_lshlrev_b32_e32 v7, 6, v7
	v_and_b32_e32 v10, 48, v9
	v_lshlrev_b32_e32 v8, 9, v8
	v_add_u32_e32 v166, s4, v5
	v_or3_b32 v6, v6, v7, v10
	v_or3_b32 v7, v8, v7, v10
	v_lshlrev_b32_e32 v8, 3, v1
	v_and_b32_e32 v5, 0xc0, v5
	v_lshlrev_b32_e32 v10, 1, v254
	v_ashrrev_i32_e32 v144, 3, v254
	v_and_or_b32 v5, v8, 24, v5
	v_and_b32_e32 v10, 32, v10
	v_and_b32_e32 v8, 0x100, v8
	v_and_b32_e32 v4, 56, v4
	v_or3_b32 v5, v5, v10, v8
	v_lshlrev_b32_e32 v8, 8, v142
	v_and_b32_e32 v10, 0x70, v254
	v_lshlrev_b32_e32 v11, 8, v11
	v_lshlrev_b32_e32 v12, 4, v144
	v_bfe_u32 v3, v254, 5, 1
	v_bitop3_b32 v8, v9, v8, v10 bitop3:0xde
	v_bitop3_b32 v9, v9, v11, v10 bitop3:0xde
	v_lshlrev_b32_e32 v10, 7, v144
	v_lshlrev_b32_e32 v11, 1, v4
	v_and_b32_e32 v12, 0x70, v12
	v_and_b32_e32 v188, 31, v254
	s_cmp_lg_u32 0, -1
	v_bitop3_b32 v168, v11, v10, v12 bitop3:0xde
	v_lshlrev_b32_e32 v169, 4, v3
	v_lshlrev_b32_e32 v10, 4, v254
	v_lshlrev_b32_e32 v0, 3, v3
	s_cselect_b32 s6, 0, 0
	v_lshlrev_b32_e32 v3, 8, v188
	v_and_b32_e32 v10, 0x70, v10
	v_or_b32_e32 v12, 32, v169
	v_or_b32_e32 v14, 64, v169
	v_or_b32_e32 v16, 0x60, v169
	v_or_b32_e32 v18, 0x80, v169
	v_or_b32_e32 v19, 0xa0, v169
	v_or_b32_e32 v20, 0xc0, v169
	v_or_b32_e32 v21, 0xe0, v169
	v_mov_b32_e32 v141, 0
	v_add_u32_e32 v167, s6, v5
	v_ashrrev_i32_e32 v143, 31, v142
	v_bitop3_b32 v11, v169, v3, v10 bitop3:0xde
	v_bitop3_b32 v13, v12, v3, v10 bitop3:0xde
	v_bitop3_b32 v15, v14, v3, v10 bitop3:0xde
	v_bitop3_b32 v17, v16, v3, v10 bitop3:0xde
	v_bitop3_b32 v18, v18, v3, v10 bitop3:0xde
	v_bitop3_b32 v19, v19, v3, v10 bitop3:0xde
	v_bitop3_b32 v20, v20, v3, v10 bitop3:0xde
	v_bitop3_b32 v3, v21, v3, v10 bitop3:0xde
	v_lshlrev_b32_e32 v21, 7, v188
	s_addk_i32 s6, 0x4000
	s_add_i32 s45, 0, 0x10000
	s_mov_b32 s9, 0
	v_lshl_add_u64 v[146:147], v[142:143], 0, 32
	v_ashrrev_i32_e32 v145, 31, v144
	v_bitop3_b32 v170, v169, v21, v10 bitop3:0xde
	v_bitop3_b32 v171, v12, v21, v10 bitop3:0xde
	v_bitop3_b32 v172, v14, v21, v10 bitop3:0xde
	v_bitop3_b32 v173, v16, v21, v10 bitop3:0xde
	v_cmp_gt_u32_e64 s[4:5], 32, v1
	s_movk_i32 s43, 0x4000
	v_add_u32_e32 v174, s6, v5
	s_movk_i32 s44, 0xc00
	v_lshlrev_b32_e32 v148, 1, v0
	v_lshlrev_b32_e32 v150, 1, v2
	v_lshlrev_b32_e32 v152, 1, v4
	v_mov_b32_e32 v153, v141
	s_mov_b32 s46, 0x42ddb3d8
	s_mov_b32 s26, 0x3dd53b94
	s_movk_i32 s47, 0x1000
	s_movk_i32 s48, 0x5000
	s_mov_b32 s49, 0x8000
	s_mov_b32 s50, 0x9000
	s_mov_b32 s51, 0xc000
	s_mov_b32 s58, 0xd000
	v_mov_b32_e32 v149, v141
	v_mov_b32_e32 v151, v141
	v_add_u32_e32 v175, 0, v6
	v_add_u32_e32 v176, 0, v7
	v_add_u32_e32 v177, 0, v8
	v_add_u32_e32 v178, 0, v9
	v_add_u32_e32 v179, s45, v168
	v_add_u32_e32 v180, 0, v11
	v_add_u32_e32 v181, 0, v13
	v_add_u32_e32 v182, 0, v15
	v_add_u32_e32 v183, 0, v17
	v_add_u32_e32 v184, 0, v18
	v_add_u32_e32 v185, 0, v19
	v_add_u32_e32 v186, 0, v20
	v_add_u32_e32 v187, 0, v3
	v_and_b32_e32 v190, 15, v188
	v_lshlrev_b32_e32 v190, 4, v190
	v_xor_b32_e32 v190, v190, v169
	v_lshlrev_b32_e32 v192, 8, v188
	v_mov_b32_e32 v191, v190
	v_or_b32_e32 v180, v192, v191
	v_xor_b32_e32 v191, 0x20, v190
	v_or_b32_e32 v181, v192, v191
	v_xor_b32_e32 v191, 0x40, v190
	v_or_b32_e32 v182, v192, v191
	v_xor_b32_e32 v191, 0x60, v190
	v_or_b32_e32 v183, v192, v191
	v_xor_b32_e32 v191, 0x80, v190
	v_or_b32_e32 v184, v192, v191
	v_xor_b32_e32 v191, 0xa0, v190
	v_or_b32_e32 v185, v192, v191
	v_xor_b32_e32 v191, 0xc0, v190
	v_or_b32_e32 v186, v192, v191
	v_xor_b32_e32 v191, 0xe0, v190
	v_or_b32_e32 v187, v192, v191
	v_bfe_u32 v190, v188, 1, 3
	v_lshlrev_b32_e32 v190, 4, v190
	v_xor_b32_e32 v190, v190, v169
	v_lshlrev_b32_e32 v192, 7, v188
	v_mov_b32_e32 v191, v190
	v_add_u32_e32 v170, v192, v191
	v_xor_b32_e32 v191, 0x20, v190
	v_add_u32_e32 v171, v192, v191
	v_xor_b32_e32 v191, 0x40, v190
	v_add_u32_e32 v172, v192, v191
	v_xor_b32_e32 v191, 0x60, v190
	v_add_u32_e32 v173, v192, v191
	v_and_b32_e32 v190, 15, v142
	v_and_b32_e32 v191, 15, v254
	v_xor_b32_e32 v190, v190, v191
	v_lshlrev_b32_e32 v190, 4, v190
	v_lshl_add_u32 v177, v142, 8, v190
	v_add_u32_e32 v178, 0x2000, v177
	v_bfe_u32 v190, v144, 1, 3
	v_and_b32_e32 v191, 7, v254
	v_xor_b32_e32 v190, v190, v191
	v_lshlrev_b32_e32 v190, 4, v190
	v_lshl_add_u32 v168, v144, 7, v190
	v_add_u32_e32 v179, s45, v168
	s_branch .LBB0_2007

.LBB0_2011:
	s_ashr_i32 s6, s11, 3
	s_lshl_b32 s60, s6, 8
	s_lshl_b32 s61, s6, 12
	s_lshl_b32 s6, s10, 8
	s_and_b32 s6, s6, 0xf00
	s_or_b32 s28, s61, s6
	s_add_i32 s8, s60, 0x4000
	s_and_b32 s12, s11, 7
	s_ashr_i32 s29, s28, 31
	s_mul_i32 s7, s28, 0xc00
	s_mul_hi_i32 s6, s28, 0xc00
	s_add_u32 s7, s35, s7
	s_addc_u32 s6, s36, s6
	s_mul_i32 s13, s12, 0x180
	s_add_u32 s10, s7, s13
	s_addc_u32 s11, s6, 0
	s_add_u32 s6, s37, s13
	s_addc_u32 s7, s38, 0
	s_lshl_b32 s59, s12, 7
	s_lshl_b32 s12, s12, 8
	s_add_u32 s30, s39, s12
	v_readfirstlane_b32 s62, v254
	s_addc_u32 s31, s40, 0
	s_ashr_i32 s12, s62, 6
	s_lshl_b32 s82, s12, 10
	s_mov_b32 s72, s6
	s_and_b32 s73, s7, 0xffff
	s_mov_b32 s74, 0x7ffffff0
	s_mov_b32 s75, 0x20000
	s_mov_b32 s76, s30
	s_and_b32 s77, s31, 0xffff
	s_mov_b32 s78, 0x7ffffff0
	s_mov_b32 s79, 0x20000
	v_lshl_add_u64 v[26:27], s[8:9], 0, v[142:143]
	v_lshl_add_u64 v[28:29], v[146:147], 0, s[8:9]
	v_lshl_or_b32 v2, s12, 5, v188
	v_mov_b64_e32 v[0:1], s[10:11]
	v_lshlrev_b64 v[16:17], 11, v[26:27]
	v_lshlrev_b64 v[18:19], 11, v[28:29]
	v_mad_i64_i32 v[0:1], s[10:11], v2, s44, v[0:1]
	v_lshl_add_u64 v[16:17], s[30:31], 0, v[16:17]
	v_lshl_add_u64 v[18:19], s[30:31], 0, v[18:19]
	v_lshl_add_u64 v[38:39], v[0:1], 0, v[148:149]
	v_lshl_add_u64 v[16:17], v[16:17], 0, v[150:151]
	v_lshl_add_u64 v[22:23], v[18:19], 0, v[150:151]
	global_load_dwordx4 v[0:3], v[38:39], off offset:256
	global_load_dwordx4 v[4:7], v[38:39], off offset:288
	global_load_dwordx4 v[8:11], v[38:39], off offset:320
	global_load_dwordx4 v[12:15], v[38:39], off offset:352
	global_load_dwordx4 v[18:21], v[16:17], off
	s_nop 0
	global_load_dwordx4 v[22:25], v[22:23], off
	v_mov_b64_e32 v[16:17], s[6:7]
	v_mad_u64_u32 v[30:31], s[10:11], v26, s44, v[16:17]
	v_mad_i32_i24 v31, v27, s44, v31
	v_lshl_add_u64 v[26:27], v[30:31], 0, v[150:151]
	v_mad_u64_u32 v[30:31], s[10:11], v28, s44, v[16:17]
	v_mad_i32_i24 v31, v29, s44, v31
	v_lshl_add_u64 v[30:31], v[30:31], 0, v[150:151]
	v_lshl_add_u64 v[34:35], s[8:9], 0, v[144:145]
	global_load_dwordx4 v[26:29], v[26:27], off
	s_nop 0
	global_load_dwordx4 v[30:33], v[30:31], off
	v_mad_u64_u32 v[36:37], s[10:11], v34, s44, v[16:17]
	v_mad_i32_i24 v37, v35, s44, v37
	v_lshl_add_u64 v[34:35], v[36:37], 0, v[152:153]
	global_load_dwordx4 v[34:37], v[34:35], off offset:256
	s_nop 0
	global_load_dwordx4 v[124:127], v[38:39], off
	global_load_dwordx4 v[120:123], v[38:39], off offset:32
	global_load_dwordx4 v[116:119], v[38:39], off offset:64
	global_load_dwordx4 v[112:115], v[38:39], off offset:96
	global_load_dwordx4 v[108:111], v[38:39], off offset:128
	global_load_dwordx4 v[104:107], v[38:39], off offset:160
	global_load_dwordx4 v[100:103], v[38:39], off offset:192
	global_load_dwordx4 v[96:99], v[38:39], off offset:224
	s_lshl_b32 s8, s12, 12
	v_add_u32_e32 v190, s8, v166
	v_add_u32_e32 v191, s45, v170
	v_add_u32_e32 v192, s45, v171
	v_add_u32_e32 v193, s45, v172
	v_add_u32_e32 v194, s45, v173
	s_mov_b32 s8, s9
	s_mov_b32 s10, s9
	s_mov_b32 s11, s9
	s_mov_b32 s12, s9
	s_mov_b32 s13, s9
	s_mov_b32 s14, s9
	s_mov_b32 s15, s9
	s_mov_b32 s16, s9
	s_mov_b32 s17, s9
	s_mov_b32 s18, s9
	s_mov_b32 s19, s9
	s_mov_b32 s20, s9
	s_mov_b32 s21, s9
	s_mov_b32 s22, s9
	s_mov_b32 s23, s9
	v_add_u32_e32 v195, 0, v168
	v_mov_b32_e32 v140, 0
	v_add_u32_e32 v196, 0x12000, v195
	v_lshrrev_b32_e32 v156, 4, v254
	v_and_b32_e32 v157, 15, v156
	v_and_b32_e32 v159, 15, v254
	v_xor_b32_e32 v157, v157, v159
	v_lshlrev_b32_e32 v157, 4, v157
	v_mad_u32_u24 v154, v156, s44, v157
	v_lshrrev_b32_e32 v156, 3, v254
	v_bfe_u32 v157, v254, 4, 3
	v_and_b32_e32 v159, 7, v254
	v_xor_b32_e32 v157, v157, v159
	v_lshlrev_b32_e32 v157, 4, v157
	v_add_u32_e32 v157, 0x100, v157
	v_mad_u32_u24 v155, v156, s44, v157
	v_and_b32_e32 v158, 3, v254
	v_lshlrev_b32_e32 v158, 4, v158
	v_bfe_u32 v156, v254, 5, 2
	v_lshl_or_b32 v158, v156, 6, v158
	v_bfe_u32 v156, v254, 2, 2
	v_lshl_or_b32 v158, v156, 11, v158
	v_bfe_u32 v156, v254, 7, 1
	v_lshl_or_b32 v158, v156, 13, v158
	v_bfe_u32 v156, v254, 4, 1
	v_lshl_or_b32 v158, v156, 14, v158
	v_bfe_u32 v156, v254, 8, 1
	v_lshl_or_b32 v158, v156, 15, v158
	s_waitcnt vmcnt(16)
	ds_write_b128 v190, v[0:3]
	s_waitcnt vmcnt(15)
	ds_write_b128 v190, v[4:7] offset:1024
	s_waitcnt vmcnt(14)
	ds_write_b128 v190, v[8:11] offset:2048
	s_waitcnt vmcnt(13)
	ds_write_b128 v190, v[12:15] offset:3072
	s_waitcnt vmcnt(0)
	s_waitcnt vmcnt(12)
	ds_write_b128 v175, v[18:21]
	s_waitcnt vmcnt(11)
	ds_write_b128 v176, v[22:25]
	s_waitcnt vmcnt(10)
	ds_write_b128 v177, v[26:29] offset:32768
	s_waitcnt vmcnt(9)
	ds_write_b128 v178, v[30:33] offset:32768
	s_waitcnt vmcnt(8)
	ds_write_b128 v179, v[34:37]
	s_waitcnt lgkmcnt(0)
	s_barrier
	ds_read_b128 v[0:3], v180 offset:32768
	ds_read_b128 v[4:7], v180 offset:40960
	s_waitcnt vmcnt(7) lgkmcnt(1)
	v_mfma_f32_32x32x16_bf16 v[48:63], v[0:3], v[124:127], 0
	s_waitcnt lgkmcnt(0)
	v_mfma_f32_32x32x16_bf16 v[64:79], v[4:7], v[124:127], 0
	ds_read_b128 v[0:3], v181 offset:32768
	ds_read_b128 v[4:7], v181 offset:40960
	s_waitcnt vmcnt(6) lgkmcnt(1)
	v_mfma_f32_32x32x16_bf16 v[48:63], v[0:3], v[120:123], v[48:63]
	s_waitcnt lgkmcnt(0)
	v_mfma_f32_32x32x16_bf16 v[64:79], v[4:7], v[120:123], v[64:79]
	ds_read_b128 v[0:3], v182 offset:32768
	ds_read_b128 v[4:7], v182 offset:40960
	s_waitcnt vmcnt(5) lgkmcnt(1)
	v_mfma_f32_32x32x16_bf16 v[48:63], v[0:3], v[116:119], v[48:63]
	s_waitcnt lgkmcnt(0)
	v_mfma_f32_32x32x16_bf16 v[64:79], v[4:7], v[116:119], v[64:79]
	ds_read_b128 v[0:3], v183 offset:32768
	ds_read_b128 v[4:7], v183 offset:40960
	s_waitcnt vmcnt(4) lgkmcnt(1)
	v_mfma_f32_32x32x16_bf16 v[48:63], v[0:3], v[112:115], v[48:63]
	s_waitcnt lgkmcnt(0)
	v_mfma_f32_32x32x16_bf16 v[64:79], v[4:7], v[112:115], v[64:79]
	ds_read_b128 v[0:3], v184 offset:32768
	ds_read_b128 v[4:7], v184 offset:40960
	s_waitcnt vmcnt(3) lgkmcnt(1)
	v_mfma_f32_32x32x16_bf16 v[48:63], v[0:3], v[108:111], v[48:63]
	s_waitcnt lgkmcnt(0)
	v_mfma_f32_32x32x16_bf16 v[64:79], v[4:7], v[108:111], v[64:79]
	ds_read_b128 v[0:3], v185 offset:32768
	ds_read_b128 v[4:7], v185 offset:40960
	s_waitcnt vmcnt(2) lgkmcnt(1)
	v_mfma_f32_32x32x16_bf16 v[48:63], v[0:3], v[104:107], v[48:63]
	s_waitcnt lgkmcnt(0)
	v_mfma_f32_32x32x16_bf16 v[64:79], v[4:7], v[104:107], v[64:79]
	ds_read_b128 v[0:3], v186 offset:32768
	ds_read_b128 v[4:7], v186 offset:40960
	s_waitcnt vmcnt(1) lgkmcnt(1)
	v_mfma_f32_32x32x16_bf16 v[48:63], v[0:3], v[100:103], v[48:63]
	s_waitcnt lgkmcnt(0)
	v_mfma_f32_32x32x16_bf16 v[64:79], v[4:7], v[100:103], v[64:79]
	ds_read_b128 v[0:3], v187 offset:32768
	ds_read_b128 v[4:7], v187 offset:40960
	s_waitcnt vmcnt(0) lgkmcnt(1)
	v_mfma_f32_32x32x16_bf16 v[48:63], v[0:3], v[96:99], v[48:63]
	s_waitcnt lgkmcnt(0)
	v_mfma_f32_32x32x16_bf16 v[64:79], v[4:7], v[96:99], v[64:79]
	ds_read_b128 v[0:3], v191
	ds_read_b128 v[4:7], v190
	ds_read_b128 v[8:11], v191 offset:4096
	ds_read_b128 v[12:15], v190 offset:1024
	s_waitcnt lgkmcnt(2)
	v_mfma_f32_32x32x16_bf16 v[48:63], v[0:3], v[4:7], v[48:63]
	s_waitcnt lgkmcnt(1)
	v_mfma_f32_32x32x16_bf16 v[64:79], v[8:11], v[4:7], v[64:79]
	ds_read_b128 v[0:3], v192
	ds_read_b128 v[4:7], v192 offset:4096
	s_waitcnt lgkmcnt(1)
	v_mfma_f32_32x32x16_bf16 v[48:63], v[0:3], v[12:15], v[48:63]
	s_waitcnt lgkmcnt(0)
	v_mfma_f32_32x32x16_bf16 v[64:79], v[4:7], v[12:15], v[64:79]
	ds_read_b128 v[0:3], v193
	ds_read_b128 v[4:7], v190 offset:2048
	ds_read_b128 v[8:11], v193 offset:4096
	ds_read_b128 v[18:21], v190 offset:3072
	ds_read_b128 v[22:25], v194 offset:4096
	s_waitcnt lgkmcnt(3)
	v_mfma_f32_32x32x16_bf16 v[48:63], v[0:3], v[4:7], v[48:63]
	ds_read_b128 v[0:3], v194
	s_waitcnt lgkmcnt(3)
	v_mfma_f32_32x32x16_bf16 v[64:79], v[8:11], v[4:7], v[64:79]
	s_waitcnt lgkmcnt(0)
	v_mfma_f32_32x32x16_bf16 v[48:63], v[0:3], v[18:21], v[48:63]
	v_mov_b64_e32 v[0:1], s[8:9]
	v_mov_b64_e32 v[2:3], s[10:11]
	v_mov_b64_e32 v[4:5], s[12:13]
	v_mov_b64_e32 v[6:7], s[14:15]
	v_mov_b64_e32 v[8:9], s[16:17]
	v_mov_b64_e32 v[10:11], s[18:19]
	v_mov_b64_e32 v[12:13], s[20:21]
	v_mfma_f32_32x32x16_bf16 v[64:79], v[22:25], v[18:21], v[64:79]
	s_nop 3
	v_max_f32_e32 v18, v49, v49
	v_max_f32_e32 v19, v48, v48
	v_max_f32_e32 v18, v19, v18
	v_max3_f32 v18, v18, v50, v51
	v_max3_f32 v18, v18, v52, v53
	v_max3_f32 v18, v18, v54, v55
	v_max3_f32 v18, v18, v56, v57
	v_max3_f32 v18, v18, v58, v59
	v_max3_f32 v18, v18, v60, v61
	v_max3_f32 v18, v18, v62, v63
	v_max3_f32 v18, v18, v64, v65
	v_max3_f32 v18, v18, v66, v67
	v_max3_f32 v18, v18, v68, v69
	v_max3_f32 v18, v18, v70, v71
	v_max3_f32 v18, v18, v72, v73
	v_max3_f32 v18, v18, v74, v75
	v_max3_f32 v18, v18, v76, v77
	v_max3_f32 v18, v18, v78, v79
	v_mov_b32_e32 v19, v18
	s_nop 1
	v_permlane32_swap_b32_e32 v18, v19
	v_mov_b64_e32 v[14:15], s[22:23]
	s_and_b32 s8, s62, 0x3fffffc0
	v_max_f32_e32 v19, v19, v19
	v_max_f32_e32 v18, v18, v18
	s_lshl_b32 s8, s8, 2
	v_max_f32_e32 v18, v18, v19
	s_add_i32 s12, s8, 0
	v_add_f32_e32 v19, 0x7149f2ca, v18
	s_add_i32 s12, s12, 0x14000
	v_cmp_ge_f32_e32 vcc, s46, v19
	s_cmp_eq_u64 vcc, exec
	s_cselect_b64 vcc, -1, 0
	s_add_i32 s8, s60, 0x4040
	v_max_f32_e32 v128, 0xf149f2ca, v18
	v_lshl_add_u64 v[18:19], s[8:9], 0, v[142:143]
	v_lshl_add_u64 v[20:21], v[146:147], 0, s[8:9]
	v_lshl_add_u64 v[22:23], s[8:9], 0, v[144:145]
	v_lshlrev_b64 v[24:25], 11, v[18:19]
	v_lshlrev_b64 v[26:27], 11, v[20:21]
	v_mad_u64_u32 v[28:29], s[10:11], v18, s44, v[16:17]
	v_mad_u64_u32 v[30:31], s[10:11], v20, s44, v[16:17]
	v_mad_u64_u32 v[16:17], s[10:11], v22, s44, v[16:17]
	v_lshl_add_u64 v[24:25], s[30:31], 0, v[24:25]
	v_lshl_add_u64 v[26:27], s[30:31], 0, v[26:27]
	v_mad_i32_i24 v29, v19, s44, v29
	v_mad_i32_i24 v31, v21, s44, v31
	v_mad_i32_i24 v17, v23, s44, v17
	v_lshl_add_u64 v[18:19], v[24:25], 0, v[150:151]
	v_lshl_add_u64 v[20:21], v[26:27], 0, v[150:151]
	v_lshl_add_u64 v[22:23], v[28:29], 0, v[150:151]
	v_lshl_add_u64 v[24:25], v[30:31], 0, v[150:151]
	v_lshl_add_u64 v[16:17], v[16:17], 0, v[152:153]
	global_load_dwordx4 v[80:83], v[18:19], off
	global_load_dwordx4 v[84:87], v[20:21], off
	global_load_dwordx4 v[88:91], v[22:23], off
	global_load_dwordx4 v[92:95], v[24:25], off
	global_load_dwordx4 v[200:203], v[16:17], off offset:256
	v_sub_f32_e32 v129, 0xf149f2ca, v128
	v_mul_f32_e32 v129, 0x3dd53b94, v129
	v_exp_f32_e32 v164, v129
	v_mov_b32_e32 v129, 0xf149f2ca
	v_cndmask_b32_e32 v198, v128, v129, vcc
	v_mul_f32_e32 v138, 0xbdd53b94, v198
	v_mov_b32_e32 v165, v138
	v_fmamk_f32 v48, v48, 0x3dd53b94, v138
	v_fmamk_f32 v49, v49, 0x3dd53b94, v138
	v_fmamk_f32 v50, v50, 0x3dd53b94, v138
	v_fmamk_f32 v51, v51, 0x3dd53b94, v138
	v_fmamk_f32 v52, v52, 0x3dd53b94, v138
	v_fmamk_f32 v53, v53, 0x3dd53b94, v138
	v_fmamk_f32 v54, v54, 0x3dd53b94, v138
	v_fmamk_f32 v55, v55, 0x3dd53b94, v138
	v_fmamk_f32 v56, v56, 0x3dd53b94, v138
	v_fmamk_f32 v57, v57, 0x3dd53b94, v138
	v_fmamk_f32 v58, v58, 0x3dd53b94, v138
	v_fmamk_f32 v59, v59, 0x3dd53b94, v138
	v_fmamk_f32 v60, v60, 0x3dd53b94, v138
	v_fmamk_f32 v61, v61, 0x3dd53b94, v138
	v_fmamk_f32 v62, v62, 0x3dd53b94, v138
	v_fmac_f32_e32 v165, 0x3dd53b94, v63
	v_exp_f32_e32 v222, v48
	v_exp_f32_e32 v224, v49
	v_exp_f32_e32 v220, v50
	v_exp_f32_e32 v223, v51
	v_exp_f32_e32 v219, v52
	v_exp_f32_e32 v221, v53
	v_exp_f32_e32 v217, v54
	v_exp_f32_e32 v218, v55
	v_exp_f32_e32 v212, v56
	v_exp_f32_e32 v214, v57
	v_exp_f32_e32 v211, v58
	v_exp_f32_e32 v213, v59
	v_exp_f32_e32 v208, v60
	v_exp_f32_e32 v210, v61
	v_exp_f32_e32 v207, v62
	v_exp_f32_e32 v209, v165
	s_waitcnt vmcnt(0)
	v_mov_b64_e32 v[46:47], v[14:15]
	v_mov_b64_e32 v[30:31], v[14:15]
	v_mov_b64_e32 v[62:63], v[14:15]
	s_mov_b32 s8, -1
	v_mov_b64_e32 v[44:45], v[12:13]
	v_mov_b64_e32 v[42:43], v[10:11]
	v_mov_b64_e32 v[40:41], v[8:9]
	v_mov_b64_e32 v[38:39], v[6:7]
	v_mov_b64_e32 v[36:37], v[4:5]
	v_mov_b64_e32 v[34:35], v[2:3]
	v_mov_b64_e32 v[32:33], v[0:1]
	v_mov_b64_e32 v[28:29], v[12:13]
	v_mov_b64_e32 v[26:27], v[10:11]
	v_mov_b64_e32 v[24:25], v[8:9]
	v_mov_b64_e32 v[22:23], v[6:7]
	v_mov_b64_e32 v[20:21], v[4:5]
	v_mov_b64_e32 v[18:19], v[2:3]
	v_mov_b64_e32 v[16:17], v[0:1]
	v_lshl_add_u32 v189, v188, 2, s12
	s_add_i32 s13, s60, 0x4080
	s_add_i32 s83, s60, 0x4040
	s_sub_i32 s14, s61, 64
	v_pk_fma_f32 v[134:135], v[78:79], s[26:27], v[138:139] op_sel_hi:[1,0,0]
	v_pk_fma_f32 v[160:161], v[76:77], s[26:27], v[138:139] op_sel_hi:[1,0,0]
	v_pk_fma_f32 v[162:163], v[74:75], s[26:27], v[138:139] op_sel_hi:[1,0,0]
	v_pk_fma_f32 v[128:129], v[72:73], s[26:27], v[138:139] op_sel_hi:[1,0,0]
	v_pk_fma_f32 v[130:131], v[70:71], s[26:27], v[138:139] op_sel_hi:[1,0,0]
	v_pk_fma_f32 v[132:133], v[68:69], s[26:27], v[138:139] op_sel_hi:[1,0,0]
	v_pk_fma_f32 v[136:137], v[66:67], s[26:27], v[138:139] op_sel_hi:[1,0,0]
	v_pk_fma_f32 v[138:139], v[64:65], s[26:27], v[138:139] op_sel_hi:[1,0,0]
	v_cndmask_b32_e64 v197, v164, 1.0, vcc
	v_mov_b64_e32 v[60:61], v[12:13]
	v_mov_b64_e32 v[58:59], v[10:11]
	v_mov_b64_e32 v[56:57], v[8:9]
	v_mov_b64_e32 v[54:55], v[6:7]
	v_mov_b64_e32 v[52:53], v[4:5]
	v_mov_b64_e32 v[50:51], v[2:3]
	v_mov_b64_e32 v[48:49], v[0:1]
	s_waitcnt vmcnt(4)
	ds_write_b128 v175, v[80:83] offset:16384
	s_waitcnt vmcnt(3)
	ds_write_b128 v176, v[84:87] offset:16384
	s_waitcnt vmcnt(2)
	ds_write_b128 v177, v[88:91] offset:49152
	s_waitcnt vmcnt(1)
	ds_write_b128 v178, v[92:95] offset:49152
	s_waitcnt vmcnt(0)
	ds_write_b128 v196, v[200:203]
	s_waitcnt lgkmcnt(0)
	s_barrier
